# v10 + P5: static priority raise for waves 4..7 (reset at P6 start)
# speedup vs baseline: 1.0096x; 1.0020x over previous
.LBB0_1095:
	s_cmp_lt_i32 s92, 6
	s_cselect_b64 s[0:1], -1, 0
	s_cmp_gt_i32 s93, 5
	s_cselect_b64 s[2:3], -1, 0
	s_and_b64 s[0:1], s[0:1], s[2:3]
	s_andn2_b64 vcc, exec, s[0:1]
	s_cbranch_vccnz .LBB0_1198
	v_readfirstlane_b32 s98, v0
	s_bitcmp1_b32 s98, 8
	s_cbranch_scc0 .Lp5_noprio
	s_setprio 1

.LBB0_1198:
	s_setprio 0
	s_cmp_lt_i32 s92, 7
	s_cselect_b64 s[0:1], -1, 0
	s_cmp_gt_i32 s93, 6
	s_cselect_b64 s[2:3], -1, 0
	s_and_b64 s[0:1], s[0:1], s[2:3]
	s_andn2_b64 vcc, exec, s[0:1]
	s_cbranch_vccnz .LBB0_1918
	v_mov_b32_e32 v2, v0
	s_nop 0
	v_readfirstlane_b32 s0, v2
	s_ashr_i32 s12, s0, 6
	s_lshl_b32 s0, s90, 3
	s_add_i32 s3, s12, s0
	s_cmpk_eq_i32 s84, 0x100
	s_cselect_b32 s98, 1, 0
	s_and_b32 s101, s3, s98
	s_xor_b32 s100, s101, s98
	s_lshl_b32 s100, s100, 1
	s_add_i32 s100, s100, 1
	s_sub_i32 s101, 4, s101
	s_lshl_b32 s99, 0x400, s98
	s_cmp_lt_i32 s3, s99
	s_waitcnt vmcnt(0)
	v_and_b32_e32 v50, 63, v2
	s_cbranch_scc1 .LBB0_1201
	s_lshl_b32 s2, s12, 14
	s_lshl_b32 s35, s84, 3
	v_mov_b32_e32 v51, 0
	s_cbranch_execz .LBB0_1202
	s_branch .LBB0_1220
